# early buffer_wbl2 by CUs that finish a phase with a tile to spare (A2/A6/A8/F1/F2 exits), on top of v040
# baseline (speedup 1.0000x reference)
.LBB0_686:
	s_add_i32 s36, s84, 2
	s_cmp_lt_i32 s36, s29
	s_cselect_b64 s[4:5], -1, 0
	s_and_b64 s[6:7], s[18:19], s[4:5]
	s_mov_b32 s85, s84
	s_andn2_b64 vcc, exec, s[6:7]
	s_cbranch_vccnz .LBB0_740
	s_waitcnt lgkmcnt(0)
	s_mov_b64 s[8:9], s[74:75]
	s_getreg_b32 s10, hwreg(HW_REG_XCC_ID, 0, 4)
	s_waitcnt vmcnt(0)
	s_waitcnt vmcnt(0)
	s_barrier
	s_mov_b64 s[6:7], exec
	v_readlane_b32 s12, v254, 1
	v_readlane_b32 s13, v254, 2
	s_and_b64 s[12:13], s[6:7], s[12:13]
	s_mov_b64 exec, s[12:13]
	s_cbranch_execz .LBB0_739
	v_readlane_b32 s11, v254, 0
	s_nop 3
	s_cmp_lt_u32 s11, 56
	s_cbranch_scc1 .Lwb_a2_skip
	buffer_wbl2 sc1
	s_waitcnt vmcnt(0)
.Lwb_a2_skip:
	v_readlane_b32 s11, v254, 15
	s_load_dwordx2 s[8:9], s[8:9], 0xd8
	s_waitcnt vmcnt(0) expcnt(0) lgkmcnt(0)
	v_mov_b32_e32 v1, s11
	ds_read_b32 v4, v1
	v_readlane_b32 s11, v254, 16
	s_and_b32 s62, s10, 15
	s_waitcnt lgkmcnt(0)
	v_cmp_ne_u32_e32 vcc, 0, v4
	v_mov_b32_e32 v1, s11
	ds_read_b32 v2, v1
	s_cbranch_vccnz .LBB0_703
	v_readlane_b32 s10, v254, 3
	v_readlane_b32 s11, v254, 4
	s_load_dwordx2 s[14:15], s[10:11], 0x0
	s_load_dword s13, s[10:11], 0x8
	s_add_u32 s10, s8, 0x4200
	s_addc_u32 s11, s9, 0
	s_add_u32 s12, s8, 0x4400
	s_waitcnt lgkmcnt(0)
	s_mul_i32 s63, s15, s14
	s_mul_i32 s63, s63, s13
	s_addc_u32 s13, s9, 0
	s_add_u32 s14, s8, 0x4500
	s_addc_u32 s15, s9, 0
	s_add_u32 s16, s8, 0x4600
	s_addc_u32 s17, s9, 0
	s_add_u32 s18, s8, 0x4700
	s_addc_u32 s19, s9, 0
	s_add_u32 s22, s8, 0x4800
	s_addc_u32 s23, s9, 0
	s_add_u32 s24, s8, 0x4900
	s_addc_u32 s25, s9, 0
	s_add_u32 s26, s8, 0x4a00
	s_addc_u32 s27, s9, 0
	s_add_u32 s34, s8, 0x4b00
	s_addc_u32 s35, s9, 0
	s_add_u32 s38, s8, 0x4c00
	s_addc_u32 s39, s9, 0
	s_add_u32 s40, s8, 0x4d00
	s_addc_u32 s41, s9, 0
	s_add_u32 s42, s8, 0x4e00
	s_addc_u32 s43, s9, 0
	s_add_u32 s44, s8, 0x4f00
	s_addc_u32 s45, s9, 0
	s_add_u32 s46, s8, 0x5000
	s_addc_u32 s47, s9, 0
	s_add_u32 s48, s8, 0x5100
	s_addc_u32 s49, s9, 0
	s_add_u32 s50, s8, 0x5200
	s_addc_u32 s51, s9, 0
	s_add_u32 s52, s8, 0x5300
	s_addc_u32 s53, s9, 0
	s_mov_b32 s64, 1
	s_branch .LBB0_691

.LBB0_1132:
	s_add_i32 s36, s85, 5
	s_cmp_lt_i32 s36, s29
	s_cselect_b64 s[4:5], -1, 0
	s_and_b64 s[6:7], s[6:7], s[4:5]
	s_andn2_b64 vcc, exec, s[6:7]
	s_cbranch_vccnz .LBB0_1186
	s_waitcnt lgkmcnt(0)
	s_mov_b64 s[8:9], s[74:75]
	s_getreg_b32 s10, hwreg(HW_REG_XCC_ID, 0, 4)
	s_waitcnt vmcnt(0)
	s_waitcnt vmcnt(0)
	s_barrier
	s_mov_b64 s[6:7], exec
	v_readlane_b32 s12, v254, 1
	v_readlane_b32 s13, v254, 2
	s_and_b64 s[12:13], s[6:7], s[12:13]
	s_mov_b64 exec, s[12:13]
	s_cbranch_execz .LBB0_1185
	v_readlane_b32 s11, v254, 0
	v_readlane_b32 s62, v255, 20
	s_nop 3
	s_cmp_lt_u32 s11, 16
	s_cbranch_scc1 .Lwb_a6_skip
	s_cmp_eq_u32 s62, 3
	s_cbranch_scc1 .Lwb_a6_skip
	buffer_wbl2 sc1
	s_waitcnt vmcnt(0)
.Lwb_a6_skip:
	v_readlane_b32 s11, v254, 15
	s_load_dwordx2 s[8:9], s[8:9], 0xd8
	s_waitcnt vmcnt(0) expcnt(0) lgkmcnt(0)
	v_mov_b32_e32 v1, s11
	ds_read_b32 v4, v1
	v_readlane_b32 s11, v254, 16
	s_and_b32 s62, s10, 15
	s_waitcnt lgkmcnt(0)
	v_cmp_ne_u32_e32 vcc, 0, v4
	v_mov_b32_e32 v1, s11
	ds_read_b32 v2, v1
	s_cbranch_vccnz .LBB0_1149
	v_readlane_b32 s10, v254, 3
	v_readlane_b32 s11, v254, 4
	s_load_dwordx2 s[14:15], s[10:11], 0x0
	s_load_dword s13, s[10:11], 0x8
	s_add_u32 s10, s8, 0x4200
	s_addc_u32 s11, s9, 0
	s_add_u32 s12, s8, 0x4400
	s_waitcnt lgkmcnt(0)
	s_mul_i32 s63, s15, s14
	s_mul_i32 s63, s63, s13
	s_addc_u32 s13, s9, 0
	s_add_u32 s14, s8, 0x4500
	s_addc_u32 s15, s9, 0
	s_add_u32 s16, s8, 0x4600
	s_addc_u32 s17, s9, 0
	s_add_u32 s18, s8, 0x4700
	s_addc_u32 s19, s9, 0
	s_add_u32 s22, s8, 0x4800
	s_addc_u32 s23, s9, 0
	s_add_u32 s24, s8, 0x4900
	s_addc_u32 s25, s9, 0
	s_add_u32 s26, s8, 0x4a00
	s_addc_u32 s27, s9, 0
	s_add_u32 s34, s8, 0x4b00
	s_addc_u32 s35, s9, 0
	s_add_u32 s38, s8, 0x4c00
	s_addc_u32 s39, s9, 0
	s_add_u32 s40, s8, 0x4d00
	s_addc_u32 s41, s9, 0
	s_add_u32 s42, s8, 0x4e00
	s_addc_u32 s43, s9, 0
	s_add_u32 s44, s8, 0x4f00
	s_addc_u32 s45, s9, 0
	s_add_u32 s46, s8, 0x5000
	s_addc_u32 s47, s9, 0
	s_add_u32 s48, s8, 0x5100
	s_addc_u32 s49, s9, 0
	s_add_u32 s50, s8, 0x5200
	s_addc_u32 s51, s9, 0
	s_add_u32 s52, s8, 0x5300
	s_addc_u32 s53, s9, 0
	s_mov_b32 s66, 1
	s_branch .LBB0_1137

.LBB0_1206:
	s_add_i32 s36, s85, 6
	s_cmp_lt_i32 s36, s29
	s_cselect_b64 s[4:5], -1, 0
	s_and_b64 s[6:7], s[6:7], s[4:5]
	s_andn2_b64 vcc, exec, s[6:7]
	s_cbranch_vccnz .LBB0_1260
	s_waitcnt lgkmcnt(0)
	s_mov_b64 s[8:9], s[74:75]
	s_getreg_b32 s10, hwreg(HW_REG_XCC_ID, 0, 4)
	s_waitcnt vmcnt(0)
	s_waitcnt vmcnt(0)
	s_barrier
	s_mov_b64 s[6:7], exec
	v_readlane_b32 s12, v254, 1
	v_readlane_b32 s13, v254, 2
	s_and_b64 s[12:13], s[6:7], s[12:13]
	s_mov_b64 exec, s[12:13]
	s_cbranch_execz .LBB0_1259
	v_readlane_b32 s11, v254, 0
	v_readlane_b32 s62, v255, 20
	s_nop 3
	s_cmp_lt_u32 s11, 16
	s_cbranch_scc1 .Lwb_a8_skip
	s_cmp_eq_u32 s62, 3
	s_cbranch_scc1 .Lwb_a8_skip
	buffer_wbl2 sc1
	s_waitcnt vmcnt(0)

.LBB0_1704:
	s_add_i32 s36, s85, 8
	s_cmp_lt_i32 s36, s29
	s_cselect_b64 s[4:5], -1, 0
	s_and_b64 s[6:7], s[12:13], s[4:5]
	s_andn2_b64 vcc, exec, s[6:7]
	s_cbranch_vccnz .LBB0_1758
	s_mov_b64 s[8:9], s[74:75]
	s_getreg_b32 s10, hwreg(HW_REG_XCC_ID, 0, 4)
	s_waitcnt vmcnt(0)
	s_waitcnt vmcnt(0)
	s_barrier
	s_mov_b64 s[6:7], exec
	v_readlane_b32 s12, v254, 1
	v_readlane_b32 s13, v254, 2
	s_and_b64 s[12:13], s[6:7], s[12:13]
	s_mov_b64 exec, s[12:13]
	s_cbranch_execz .LBB0_1757
	v_readlane_b32 s11, v254, 0
	s_nop 3
	s_cmp_lt_u32 s11, 88
	s_cbranch_scc1 .Lwb_f1_skip
	buffer_wbl2 sc1
	s_waitcnt vmcnt(0)

.LBB0_1782:
	s_add_i32 s36, s85, 9
	s_cmp_lt_i32 s36, s29
	s_cselect_b64 s[4:5], -1, 0
	s_and_b64 s[4:5], s[8:9], s[4:5]
	s_andn2_b64 vcc, exec, s[4:5]
	s_cbranch_vccnz .LBB0_1836
	s_mov_b64 s[6:7], s[74:75]
	s_getreg_b32 s8, hwreg(HW_REG_XCC_ID, 0, 4)
	s_waitcnt vmcnt(0)
	s_waitcnt vmcnt(0)
	s_barrier
	s_mov_b64 s[4:5], exec
	v_readlane_b32 s10, v254, 1
	v_readlane_b32 s11, v254, 2
	s_and_b64 s[10:11], s[4:5], s[10:11]
	s_mov_b64 exec, s[10:11]
	s_cbranch_execz .LBB0_1835
	v_readlane_b32 s9, v254, 0
	s_nop 3
	s_cmp_lt_u32 s9, 16
	s_cbranch_scc1 .Lwb_f2_skip
	buffer_wbl2 sc1
	s_waitcnt vmcnt(0)
.Lwb_f2_skip:
	v_readlane_b32 s9, v254, 15
	s_load_dwordx2 s[6:7], s[6:7], 0xd8
	s_waitcnt vmcnt(0) expcnt(0) lgkmcnt(0)
	v_mov_b32_e32 v1, s9
	ds_read_b32 v4, v1
	v_readlane_b32 s9, v254, 16
	s_and_b32 s60, s8, 15
	s_waitcnt lgkmcnt(0)
	v_cmp_ne_u32_e32 vcc, 0, v4
	v_mov_b32_e32 v1, s9
	ds_read_b32 v2, v1
	s_cbranch_vccnz .LBB0_1799
	v_readlane_b32 s8, v254, 3
	v_readlane_b32 s9, v254, 4
	s_load_dwordx2 s[12:13], s[8:9], 0x0
	s_load_dword s11, s[8:9], 0x8
	s_add_u32 s8, s6, 0x4200
	s_addc_u32 s9, s7, 0
	s_add_u32 s10, s6, 0x4400
	s_waitcnt lgkmcnt(0)
	s_mul_i32 s61, s13, s12
	s_mul_i32 s61, s61, s11
	s_addc_u32 s11, s7, 0
	s_add_u32 s12, s6, 0x4500
	s_addc_u32 s13, s7, 0
	s_add_u32 s14, s6, 0x4600
	s_addc_u32 s15, s7, 0
	s_add_u32 s16, s6, 0x4700
	s_addc_u32 s17, s7, 0
	s_add_u32 s18, s6, 0x4800
	s_addc_u32 s19, s7, 0
	s_add_u32 s22, s6, 0x4900
	s_addc_u32 s23, s7, 0
	s_add_u32 s24, s6, 0x4a00
	s_addc_u32 s25, s7, 0
	s_add_u32 s26, s6, 0x4b00
	s_addc_u32 s27, s7, 0
	s_add_u32 s34, s6, 0x4c00
	s_addc_u32 s35, s7, 0
	s_add_u32 s38, s6, 0x4d00
	s_addc_u32 s39, s7, 0
	s_add_u32 s40, s6, 0x4e00
	s_addc_u32 s41, s7, 0
	s_add_u32 s42, s6, 0x4f00
	s_addc_u32 s43, s7, 0
	s_add_u32 s44, s6, 0x5000
	s_addc_u32 s45, s7, 0
	s_add_u32 s46, s6, 0x5100
	s_addc_u32 s47, s7, 0
	s_add_u32 s48, s6, 0x5200
	s_addc_u32 s49, s7, 0
	s_add_u32 s50, s6, 0x5300
	s_addc_u32 s51, s7, 0
	s_mov_b32 s62, 1
	s_branch .LBB0_1787
